# speedup vs baseline: 1.0186x; 1.0186x over previous
.LBB0_318:
	v_mul_f32_e32 v250, v129, v229
	v_cmp_class_f32_e64 s[82:83], v228, 64
	v_add_f32_dpp v12, v180, v180 row_ror:8 row_mask:0xf bank_mask:0xf bound_ctrl:1
	v_mov_b32_e32 v61, v13
	v_cndmask_b32_e64 v46, v176, 5, s[16:17]
	v_mul_f32_e32 v251, v132, v231
	v_cmp_class_f32_e64 s[84:85], v230, 64
	v_fma_f32 v18, v250, v54, v18
	v_add_f32_dpp v12, v12, v12 row_ror:4 row_mask:0xf bank_mask:0xf bound_ctrl:1
	s_mov_b64 s[60:61], s[16:17]
	v_fma_f32 v19, v251, v54, v19
	v_cndmask_b32_e64 v250, -v130, v173, s[82:83]
	v_cndmask_b32_e64 v251, -v133, v173, s[84:85]
	v_add_f32_dpp v60, v12, v12 row_ror:2 row_mask:0xf bank_mask:0xf bound_ctrl:1
	v_mov_b32_e32 v12, 48
	v_fmac_f32_e32 v18, v250, v55
	v_fmac_f32_e32 v19, v251, v55
	v_med3_f32 v18, v18, v71, 0
	v_mov_b32_dpp v61, v60 row_ror:1 row_mask:0xf bank_mask:0xf
	s_and_saveexec_b64 s[58:59], s[10:11]
	s_cbranch_execz .LBB0_286
	v_med3_f32 v19, v19, v81, 0
	v_mul_f32_e32 v218, v9, v18
	v_mul_f32_e32 v219, v131, v19
	v_add_f32_e32 v12, v60, v61
	v_cvt_f64_f32_e32 v[248:249], v12
	v_mul_f32_e32 v250, v135, v233
	v_cmp_class_f32_e64 s[82:83], v232, 64
	v_mul_f32_e32 v251, v138, v235
	v_cmp_class_f32_e64 s[84:85], v234, 64
	v_fmac_f64_e32 v[248:249], v[0:1], v[10:11]
	v_cmp_gt_i32_e32 vcc, 1, v46
	v_mov_b32_e32 v12, 0
	v_fma_f32 v20, v250, v54, v20
	v_fma_f32 v21, v251, v54, v21
	v_cndmask_b32_e64 v250, -v136, v173, s[82:83]
	v_cndmask_b32_e64 v251, -v139, v173, s[84:85]
	v_fmac_f32_e32 v20, v250, v55
	v_cndmask_b32_e32 v1, 0, v249, vcc
	v_cndmask_b32_e32 v0, 0, v248, vcc
	s_waitcnt lgkmcnt(0)
	v_cvt_f64_f32_e32 v[248:249], v179
	v_fmac_f32_e32 v21, v251, v55
	v_med3_f32 v20, v20, v85, 0
	v_med3_f32 v21, v21, v86, 0
	v_mul_f32_e32 v220, v134, v20
	v_add_f64 v[0:1], v[0:1], v[248:249]
	v_mul_f32_e32 v221, v137, v21
	v_mul_f32_e32 v250, v141, v237
	v_cmp_class_f32_e64 s[82:83], v236, 64
	v_mul_f32_e32 v251, v144, v239
	v_cmp_class_f32_e64 s[84:85], v238, 64
	v_cmp_le_f64_e32 vcc, 1.0, v[0:1]
	v_fma_f32 v22, v250, v54, v22
	v_fma_f32 v23, v251, v54, v23
	v_cndmask_b32_e64 v250, -v142, v173, s[82:83]
	v_cndmask_b32_e64 v251, -v145, v173, s[84:85]
	v_fmac_f32_e32 v22, v250, v55
	s_lshr_b32 s11, vcc_lo, 15
	s_and_b32 s10, vcc_lo, 1
	s_and_b32 s11, s11, 2
	s_or_b32 s60, s11, s10
	s_lshr_b64 s[10:11], vcc, 30
	s_and_b32 s10, s10, 4
	s_lshr_b32 s11, vcc_hi, 13
	s_or_b32 s10, s60, s10
	s_and_b32 s11, s11, 8
	s_or_b32 s10, s10, s11
	v_lshlrev_b32_e64 v248, v163, s10
	s_and_saveexec_b64 s[10:11], s[4:5]
	v_and_b32_e32 v12, 3, v178
	v_lshl_or_b32 v12, v12, 2, v175
	v_or_b32_e32 v249, 0x10000, v248
	ds_add_rtn_u32 v12, v12, v249
	s_or_b64 exec, exec, s[10:11]
	v_fmac_f32_e32 v23, v251, v55
	v_med3_f32 v22, v22, v87, 0
	v_med3_f32 v23, v23, v88, 0
	v_mul_f32_e32 v222, v140, v22
	v_mul_f32_e32 v223, v143, v23
	v_mul_f32_e32 v250, v147, v241
	v_cmp_class_f32_e64 s[82:83], v240, 64
	v_mul_f32_e32 v251, v151, v243
	v_cmp_class_f32_e64 s[84:85], v242, 64
	v_fma_f32 v24, v250, v54, v24
	v_fma_f32 v25, v251, v54, v25
	v_cndmask_b32_e64 v250, -v148, v173, s[82:83]
	v_cndmask_b32_e64 v251, -v152, v173, s[84:85]
	v_fmac_f32_e32 v24, v250, v55
	v_fmac_f32_e32 v25, v251, v55
	v_med3_f32 v24, v24, v89, 0
	v_med3_f32 v25, v25, v90, 0
	v_mul_f32_e32 v224, v146, v24
	v_mul_f32_e32 v225, v150, v25
	v_add_u16_e32 v208, 0x1000, v208
	v_add_u16_e32 v209, 0x1000, v209
	v_add_u16_e32 v210, 0x1000, v210
	v_add_u16_e32 v211, 0x1000, v211
	v_add_u16_e32 v212, 0x1000, v212
	v_add_u16_e32 v213, 0x1000, v213
	v_add_u16_e32 v214, 0x1000, v214
	v_add_u16_e32 v215, 0x1000, v215
	s_cmp_eq_u64 s[18:19], 0
	s_cbranch_scc1 .Lmy_no89
	v_mul_f32_e32 v250, v123, v245
	v_cmp_class_f32_e64 s[82:83], v244, 64
	v_mul_f32_e32 v251, v124, v247
	v_cmp_class_f32_e64 s[84:85], v246, 64
	v_fma_f32 v26, v250, v54, v26
	v_fma_f32 v27, v251, v54, v27
	v_cndmask_b32_e64 v250, -v125, v173, s[82:83]
	v_cndmask_b32_e64 v251, -v126, v173, s[84:85]
	v_fmac_f32_e32 v26, v250, v55
	v_fmac_f32_e32 v27, v251, v55
	v_med3_f32 v26, v26, v91, 0
	v_med3_f32 v27, v27, v92, 0
	v_mul_f32_e32 v226, v121, v26
	v_mul_f32_e32 v227, v122, v27
	v_add_u16_e32 v216, 0x1000, v216
	v_add_u16_e32 v217, 0x1000, v217
